# K2 hand-rewritten: all loads issued up front, direct per-wave atomics, no second barrier
# speedup vs baseline: 1.0380x; 1.0380x over previous
.LBB0_2:
.LBB0_3:
	s_lshl_b32 s3, s2, 5
	s_and_b32 s3, s3, 0x700
	v_or_b32_e32 v1, s3, v0
	s_load_dwordx2 s[20:21], s[0:1], 0x30
	s_load_dwordx4 s[8:11], s[0:1], 0x38
	s_load_dword s3, s[0:1], 0x48
	s_load_dwordx8 s[12:19], s[0:1], 0x10
	s_waitcnt lgkmcnt(0)
	s_add_i32 s0, s8, -1
	v_min_i32_e32 v4, s0, v1
	s_add_i32 s0, s9, -1
	v_mov_b32_e32 v2, s12
	v_mov_b32_e32 v3, s13
	v_ashrrev_i32_e32 v5, 31, v4
	v_min_i32_e32 v8, s0, v1
	s_add_i32 s0, s10, -1
	v_mov_b32_e32 v6, s14
	v_mov_b32_e32 v7, s15
	v_lshl_add_u64 v[2:3], v[4:5], 4, v[2:3]
	v_ashrrev_i32_e32 v9, 31, v8
	v_min_i32_e32 v12, s0, v1
	s_add_i32 s0, s11, -1
	v_mov_b32_e32 v10, s16
	v_mov_b32_e32 v11, s17
	global_load_dword v53, v[2:3], off
	v_lshl_add_u64 v[6:7], v[8:9], 4, v[6:7]
	v_ashrrev_i32_e32 v13, 31, v12
	v_min_i32_e32 v16, s0, v1
	s_add_i32 s3, s3, -1
	v_mov_b32_e32 v14, s18
	v_mov_b32_e32 v15, s19
	global_load_dword v54, v[6:7], off
	v_lshl_add_u64 v[10:11], v[12:13], 4, v[10:11]
	v_ashrrev_i32_e32 v17, 31, v16
	v_min_i32_e32 v18, s3, v1
	global_load_dword v55, v[10:11], off
	v_lshl_add_u64 v[14:15], v[16:17], 4, v[14:15]
	v_ashrrev_i32_e32 v19, 31, v18
	global_load_dword v56, v[14:15], off
	v_lshl_add_u64 v[18:19], v[18:19], 4, s[20:21]
	global_load_dword v52, v[18:19], off
.LBB0_6:
	v_mbcnt_lo_u32_b32 v3, -1, 0
	v_mbcnt_hi_u32_b32 v3, -1, v3
	s_lshr_b32 s12, s2, 3
	s_mov_b32 s13, 0
	v_and_b32_e32 v5, 64, v3
	s_and_b32 s3, s2, 7
	s_lshl_b64 s[0:1], s[12:13], 20
	v_xor_b32_e32 v4, 16, v3
	v_add_u32_e32 v5, 64, v5
	s_waitcnt lgkmcnt(0)
	s_add_u32 s8, s4, s0
	v_cmp_lt_i32_e32 vcc, v4, v5
	v_lshrrev_b32_e32 v62, 6, v0
	s_addc_u32 s0, s5, s1
	s_lshl_b32 s12, s12, 9
	v_cndmask_b32_e32 v4, v3, v4, vcc
	s_and_b32 s9, s0, 0xffff
	v_lshlrev_b32_e32 v2, 2, v62
	v_lshlrev_b32_e32 v65, 2, v4
	v_xor_b32_e32 v4, 32, v3
	s_lshl_b64 s[4:5], s[12:13], 2
	v_and_b32_e32 v1, 63, v0
	v_cmp_lt_i32_e32 vcc, v4, v5
	v_lshl_add_u32 v66, s3, 6, v2
	s_add_u32 s4, s6, s4
	v_lshlrev_b32_e32 v2, 13, v62
	v_lshlrev_b32_e32 v63, 4, v1
	v_cndmask_b32_e32 v3, v3, v4, vcc
	v_lshlrev_b32_e32 v42, 2, v66
	v_mov_b32_e32 v43, 0
	s_addc_u32 s5, s7, s5
	v_lshl_add_u32 v2, s3, 17, v2
	s_mov_b32 s11, 0x20000
	s_mov_b32 s10, 0x100000
	v_lshlrev_b32_e32 v64, 2, v3
	v_cmp_eq_u32_e64 s[0:1], 0, v1
	v_lshl_add_u64 v[44:45], s[4:5], 0, v[42:43]
	v_lshrrev_b32_e32 v67, 2, v66
	v_or_b32_e32 v68, v2, v63
	v_mov_b32_e32 v42, v43
	v_mov_b32_e32 v2, v43
	v_mov_b32_e32 v3, v43
	v_mov_b32_e32 v4, v43
	v_mov_b32_e32 v5, v43
	v_mov_b32_e32 v6, v43
	v_mov_b32_e32 v7, v43
	v_mov_b32_e32 v8, v43
	v_mov_b32_e32 v9, v43
	s_sub_u32 s14, s2, 64
	s_cmp_lt_u32 s14, 3
	s_cbranch_scc0 .Lk1_nozero
	v_lshlrev_b32_e32 v10, 4, v0
	s_lshl_b32 s14, s14, 12
	v_add_u32_e32 v10, s14, v10
	v_add_u32_e32 v10, 0x582000, v10
	global_store_dwordx4 v10, v[2:5], s[6:7]
.Lk1_nozero:
	s_branch .LBB0_8

.LBB0_12:
.LBB0_20:
	v_mov_b32_e32 v12, 0
	v_mov_b32_e32 v13, 0
	v_mov_b32_e32 v14, 0
	v_mov_b32_dpp v12, v42 quad_perm:[1,0,3,2] row_mask:0xf bank_mask:0xf
	v_mov_b32_dpp v13, v43 quad_perm:[1,0,3,2] row_mask:0xf bank_mask:0xf
	v_pk_add_f32 v[12:13], v[42:43], v[12:13]
	v_mov_b32_e32 v15, 0
	v_mov_b32_e32 v11, 0
	v_mov_b32_dpp v14, v12 quad_perm:[2,3,0,1] row_mask:0xf bank_mask:0xf
	v_mov_b32_dpp v15, v13 quad_perm:[2,3,0,1] row_mask:0xf bank_mask:0xf
	v_pk_add_f32 v[12:13], v[12:13], v[14:15]
	v_mov_b32_e32 v14, 0
	v_mov_b32_e32 v15, 0
	v_mov_b32_e32 v10, 0
	v_mov_b32_dpp v14, v12 row_half_mirror row_mask:0xf bank_mask:0xf
	v_mov_b32_dpp v15, v13 row_half_mirror row_mask:0xf bank_mask:0xf
	v_pk_add_f32 v[12:13], v[12:13], v[14:15]
	v_lshl_or_b32 v1, v62, 11, v63
	ds_write_b128 v1, v[2:5]
	ds_write_b128 v1, v[6:9] offset:1024
	v_mov_b32_dpp v10, v12 row_mirror row_mask:0xf bank_mask:0xf
	v_mov_b32_dpp v11, v13 row_mirror row_mask:0xf bank_mask:0xf
	v_pk_add_f32 v[10:11], v[12:13], v[10:11]
	ds_bpermute_b32 v12, v65, v10
	ds_bpermute_b32 v13, v65, v11
	s_waitcnt lgkmcnt(0)
	v_pk_add_f32 v[10:11], v[10:11], v[12:13]
	ds_bpermute_b32 v12, v64, v10
	ds_bpermute_b32 v13, v64, v11
	s_and_saveexec_b64 s[4:5], s[0:1]
	s_cbranch_execz .LBB0_22
	v_lshlrev_b32_e32 v1, 3, v62
	s_waitcnt lgkmcnt(0)
	v_pk_add_f32 v[2:3], v[10:11], v[12:13]
	ds_write_b64 v1, v[2:3] offset:8192

_Z9k2_layer1PKfS0_S0_PfS1_S1_:
	s_load_dwordx8 s[4:11], s[0:1], 0x0
	s_load_dwordx4 s[12:15], s[0:1], 0x20
	s_lshr_b32 s16, s2, 5
	s_and_b32 s17, s2, 31
	s_lshl_b32 s17, s17, 4
	s_movk_i32 s18, 0x500
	v_and_b32_e32 v1, 15, v0
	v_lshrrev_b32_e32 v2, 4, v0
	v_lshl_add_u32 v3, s16, 4, v2
	v_add_u32_e32 v4, s17, v1
	v_lshlrev_b32_e32 v4, 2, v4
	v_lshl_add_u32 v5, v3, 11, v4
	v_add_u32_e32 v6, 0x40000, v5
	v_lshl_add_u32 v7, v3, 14, v4
	v_add_u32_e32 v7, 0x80000, v7
	v_add_u32_e32 v8, 0x1000, v7
	v_add_u32_e32 v9, 0x2000, v7
	v_add_u32_e32 v10, 0x3000, v7
	v_and_b32_e32 v11, 7, v1
	v_lshl_add_u32 v11, v3, 3, v11
	v_lshlrev_b32_e32 v11, 2, v11
	v_and_b32_e32 v12, 8, v1
	v_lshl_add_u32 v11, v12, 9, v11
	v_add_u32_e32 v11, 0x280000, v11
	v_lshrrev_b32_e32 v13, 6, v0
	v_bfe_u32 v14, v0, 4, 2
	v_lshl_add_u32 v15, v13, 4, v1
	v_mul_u32_u24_e32 v16, 20, v15
	v_mad_u32_u24 v16, v14, s18, v16
	v_add_u32_e32 v17, 0x1400, v16
	v_add_u32_e32 v18, 0x2800, v16
	v_add_u32_e32 v19, 0x3c00, v16
	v_lshlrev_b32_e32 v20, 2, v15
	s_waitcnt lgkmcnt(0)
	global_load_dword v24, v5, s[4:5]
	global_load_dword v25, v6, s[4:5]
	global_load_dword v26, v7, s[4:5]
	global_load_dword v27, v7, s[4:5] offset:2048
	global_load_dword v28, v8, s[4:5]
	global_load_dword v29, v8, s[4:5] offset:2048
	global_load_dword v30, v9, s[4:5]
	global_load_dword v31, v9, s[4:5] offset:2048
	global_load_dword v32, v10, s[4:5]
	global_load_dword v33, v10, s[4:5] offset:2048
	global_load_dword v34, v11, s[4:5]
	global_load_dwordx4 v[36:39], v16, s[6:7]
	global_load_dwordx4 v[40:43], v17, s[6:7]
	global_load_dwordx4 v[44:47], v18, s[6:7]
	global_load_dwordx4 v[48:51], v19, s[6:7]
	global_load_dword v52, v16, s[6:7] offset:16
	global_load_dword v53, v17, s[6:7] offset:16
	global_load_dword v54, v18, s[6:7] offset:16
	global_load_dword v55, v19, s[6:7] offset:16
	global_load_dword v56, v20, s[8:9]
	v_lshlrev_b32_e32 v21, 2, v0
	v_and_b32_e32 v22, 63, v0
	v_lshlrev_b32_e32 v22, 2, v22
	v_lshlrev_b32_e32 v23, 2, v14
	v_add_u32_e32 v23, 0xc00, v23
	v_lshlrev_b32_e32 v57, 3, v12
	v_lshl_add_u32 v57, v2, 2, v57
	v_add_u32_e32 v57, 0xc00, v57
	v_mul_u32_u24_e32 v58, 0x900000, v12
	v_sub_u32_e32 v58, 0x3b000000, v58
	s_lshl_b32 s19, s2, 4
	v_add_u32_e32 v59, s19, v1
	v_lshlrev_b32_e32 v59, 6, v59
	v_lshl_add_u32 v59, v13, 4, v59
	v_lshl_add_u32 v59, v14, 2, v59
	v_lshlrev_b32_e32 v59, 2, v59
	v_and_b32_e32 v90, 3, v1
	v_lshl_add_u32 v90, v14, 2, v90
	v_lshl_add_u32 v90, v13, 4, v90
	s_lshl_b32 s19, s16, 8
	v_lshl_add_u32 v90, v90, 2, s19
	v_mov_b32_e32 v89, 1.0
	s_mov_b32 s20, 0x01010101
	s_mov_b32 s21, 0x01010101
	s_mov_b32 s22, 0xffff
	s_mov_b32 s23, 0
	s_waitcnt vmcnt(9)
	v_add_f32_dpp v34, v34, v34 quad_perm:[1,0,3,2] row_mask:0xf bank_mask:0xf
	v_add_f32_e32 v26, v26, v27
	v_add_f32_e32 v28, v28, v29
	v_add_f32_dpp v34, v34, v34 quad_perm:[2,3,0,1] row_mask:0xf bank_mask:0xf
	v_add_f32_e32 v30, v30, v31
	v_add_f32_e32 v32, v32, v33
	v_add_f32_dpp v34, v34, v34 row_half_mirror row_mask:0xf bank_mask:0xf
	v_add_f32_e32 v26, v26, v28
	v_add_f32_e32 v30, v30, v32
	v_mul_f32_e32 v25, 0x3b000000, v25
	v_add_f32_e32 v26, v26, v30
	v_mul_f32_e32 v34, v58, v34
	v_mul_f32_e32 v26, 0x3b000000, v26
	ds_write_b32 v21, v24
	ds_write_b32 v21, v25 offset:1024
	ds_write_b32 v21, v26 offset:2048
	s_mov_b64 exec, s[20:21]
	ds_write_b32 v57, v34
	s_mov_b64 exec, -1
	s_waitcnt lgkmcnt(0)
	s_barrier
	ds_read2st64_b32 v[60:61], v22 offset0:0 offset1:1
	ds_read2st64_b32 v[62:63], v22 offset0:2 offset1:3
	ds_read2st64_b32 v[64:65], v22 offset0:4 offset1:5
	ds_read2st64_b32 v[66:67], v22 offset0:6 offset1:7
	ds_read2st64_b32 v[68:69], v22 offset0:8 offset1:9
	ds_read2st64_b32 v[70:71], v22 offset0:10 offset1:11
	ds_read2_b32 v[72:73], v23 offset0:0 offset1:16
	ds_read2_b32 v[74:75], v23 offset0:4 offset1:20
	ds_read2_b32 v[76:77], v23 offset0:8 offset1:24
	ds_read2_b32 v[78:79], v23 offset0:12 offset1:28
	s_waitcnt vmcnt(0)
	s_waitcnt lgkmcnt(9)
	v_mfma_f32_16x16x4_f32 v[80:83], v36, v60, 0
	v_mfma_f32_16x16x4_f32 v[84:87], v40, v61, 0
	s_waitcnt lgkmcnt(8)
	v_mfma_f32_16x16x4_f32 v[80:83], v44, v62, v[80:83]
	v_mfma_f32_16x16x4_f32 v[84:87], v48, v63, v[84:87]
	s_waitcnt lgkmcnt(7)
	v_mfma_f32_16x16x4_f32 v[80:83], v38, v64, v[80:83]
	v_mfma_f32_16x16x4_f32 v[84:87], v42, v65, v[84:87]
	v_cndmask_b32_e64 v88, 0, v56, s[22:23]
	s_waitcnt lgkmcnt(6)
	v_mfma_f32_16x16x4_f32 v[80:83], v46, v66, v[80:83]
	v_mfma_f32_16x16x4_f32 v[84:87], v50, v67, v[84:87]
	s_waitcnt lgkmcnt(5)
	v_mfma_f32_16x16x4_f32 v[80:83], v39, v68, v[80:83]
	v_mfma_f32_16x16x4_f32 v[84:87], v43, v69, v[84:87]
	s_waitcnt lgkmcnt(4)
	v_mfma_f32_16x16x4_f32 v[80:83], v47, v70, v[80:83]
	v_mfma_f32_16x16x4_f32 v[84:87], v51, v71, v[84:87]
	s_waitcnt lgkmcnt(0)
	v_fmac_f32_e32 v88, v37, v72
	v_fmac_f32_e32 v88, v52, v73
	v_fmac_f32_e32 v88, v41, v74
	v_fmac_f32_e32 v88, v53, v75
	v_fmac_f32_e32 v88, v45, v76
	v_fmac_f32_e32 v88, v54, v77
	v_fmac_f32_e32 v88, v49, v78
	v_fmac_f32_e32 v88, v55, v79
	s_nop 1
	v_mfma_f32_16x16x4_f32 v[80:83], v88, v89, v[80:83]
	s_nop 7
	s_nop 1
	v_add_f32_e32 v80, v80, v84
	v_add_f32_e32 v81, v81, v85
	v_add_f32_e32 v82, v82, v86
	v_add_f32_e32 v83, v83, v87
	v_max_f32_e32 v80, 0, v80
	v_max_f32_e32 v81, 0, v81
	v_max_f32_e32 v82, 0, v82
	v_max_f32_e32 v83, 0, v83
	global_store_dwordx4 v59, v[80:83], s[10:11] sc1
	v_mul_f32_e32 v84, v80, v80
	v_mul_f32_e32 v85, v81, v81
	v_mul_f32_e32 v86, v82, v82
	v_mul_f32_e32 v87, v83, v83
	v_add_f32_dpp v80, v80, v80 quad_perm:[1,0,3,2] row_mask:0xf bank_mask:0xf
	v_add_f32_dpp v81, v81, v81 quad_perm:[1,0,3,2] row_mask:0xf bank_mask:0xf
	v_add_f32_dpp v82, v82, v82 quad_perm:[1,0,3,2] row_mask:0xf bank_mask:0xf
	v_add_f32_dpp v83, v83, v83 quad_perm:[1,0,3,2] row_mask:0xf bank_mask:0xf
	v_add_f32_dpp v84, v84, v84 quad_perm:[1,0,3,2] row_mask:0xf bank_mask:0xf
	v_add_f32_dpp v85, v85, v85 quad_perm:[1,0,3,2] row_mask:0xf bank_mask:0xf
	v_add_f32_dpp v86, v86, v86 quad_perm:[1,0,3,2] row_mask:0xf bank_mask:0xf
	v_add_f32_dpp v87, v87, v87 quad_perm:[1,0,3,2] row_mask:0xf bank_mask:0xf
	v_add_f32_dpp v80, v80, v80 quad_perm:[2,3,0,1] row_mask:0xf bank_mask:0xf
	v_add_f32_dpp v81, v81, v81 quad_perm:[2,3,0,1] row_mask:0xf bank_mask:0xf
	v_add_f32_dpp v82, v82, v82 quad_perm:[2,3,0,1] row_mask:0xf bank_mask:0xf
	v_add_f32_dpp v83, v83, v83 quad_perm:[2,3,0,1] row_mask:0xf bank_mask:0xf
	v_add_f32_dpp v84, v84, v84 quad_perm:[2,3,0,1] row_mask:0xf bank_mask:0xf
	v_add_f32_dpp v85, v85, v85 quad_perm:[2,3,0,1] row_mask:0xf bank_mask:0xf
	v_add_f32_dpp v86, v86, v86 quad_perm:[2,3,0,1] row_mask:0xf bank_mask:0xf
	v_add_f32_dpp v87, v87, v87 quad_perm:[2,3,0,1] row_mask:0xf bank_mask:0xf
	v_add_f32_dpp v80, v80, v80 row_half_mirror row_mask:0xf bank_mask:0xf
	v_add_f32_dpp v81, v81, v81 row_half_mirror row_mask:0xf bank_mask:0xf
	v_add_f32_dpp v82, v82, v82 row_half_mirror row_mask:0xf bank_mask:0xf
	v_add_f32_dpp v83, v83, v83 row_half_mirror row_mask:0xf bank_mask:0xf
	v_add_f32_dpp v84, v84, v84 row_half_mirror row_mask:0xf bank_mask:0xf
	v_add_f32_dpp v85, v85, v85 row_half_mirror row_mask:0xf bank_mask:0xf
	v_add_f32_dpp v86, v86, v86 row_half_mirror row_mask:0xf bank_mask:0xf
	v_add_f32_dpp v87, v87, v87 row_half_mirror row_mask:0xf bank_mask:0xf
	v_add_f32_dpp v80, v80, v80 row_mirror row_mask:0xf bank_mask:0xf
	v_add_f32_dpp v81, v81, v81 row_mirror row_mask:0xf bank_mask:0xf
	v_add_f32_dpp v82, v82, v82 row_mirror row_mask:0xf bank_mask:0xf
	v_add_f32_dpp v83, v83, v83 row_mirror row_mask:0xf bank_mask:0xf
	v_add_f32_dpp v84, v84, v84 row_mirror row_mask:0xf bank_mask:0xf
	v_add_f32_dpp v85, v85, v85 row_mirror row_mask:0xf bank_mask:0xf
	v_add_f32_dpp v86, v86, v86 row_mirror row_mask:0xf bank_mask:0xf
	v_add_f32_dpp v87, v87, v87 row_mirror row_mask:0xf bank_mask:0xf
	s_mov_b32 s24, 0x00020002
	s_mov_b32 s25, 0x00020002
	v_cndmask_b32_e64 v80, v80, v81, s[24:25]
	s_mov_b32 s24, 0x00040004
	s_mov_b32 s25, 0x00040004
	v_cndmask_b32_e64 v80, v80, v82, s[24:25]
	s_mov_b32 s24, 0x00080008
	s_mov_b32 s25, 0x00080008
	v_cndmask_b32_e64 v80, v80, v83, s[24:25]
	s_mov_b32 s24, 0x00100010
	s_mov_b32 s25, 0x00100010
	v_cndmask_b32_e64 v80, v80, v84, s[24:25]
	s_mov_b32 s24, 0x00200020
	s_mov_b32 s25, 0x00200020
	v_cndmask_b32_e64 v80, v80, v85, s[24:25]
	s_mov_b32 s24, 0x00400040
	s_mov_b32 s25, 0x00400040
	v_cndmask_b32_e64 v80, v80, v86, s[24:25]
	s_mov_b32 s24, 0x00800080
	s_mov_b32 s25, 0x00800080
	v_cndmask_b32_e64 v80, v80, v87, s[24:25]
	s_mov_b32 s24, 0x000f000f
	s_mov_b32 s25, 0x000f000f
	s_mov_b64 exec, s[24:25]
	global_atomic_add_f32 v90, v80, s[12:13]
	s_mov_b32 s24, 0x00f000f0
	s_mov_b32 s25, 0x00f000f0
	s_mov_b64 exec, s[24:25]
	global_atomic_add_f32 v90, v80, s[14:15]
	s_endpgm

	.amdhsa_kernel _Z9k2_layer1PKfS0_S0_PfS1_S1_
		.amdhsa_group_segment_fixed_size 3712
		.amdhsa_private_segment_fixed_size 0
		.amdhsa_kernarg_size 48
		.amdhsa_user_sgpr_count 2
		.amdhsa_user_sgpr_dispatch_ptr 0
		.amdhsa_user_sgpr_queue_ptr 0
		.amdhsa_user_sgpr_kernarg_segment_ptr 1
		.amdhsa_user_sgpr_dispatch_id 0
		.amdhsa_user_sgpr_kernarg_preload_length 0
		.amdhsa_user_sgpr_kernarg_preload_offset 0
		.amdhsa_user_sgpr_private_segment_size 0
		.amdhsa_uses_dynamic_stack 0
		.amdhsa_enable_private_segment 0
		.amdhsa_system_sgpr_workgroup_id_x 1
		.amdhsa_system_sgpr_workgroup_id_y 0
		.amdhsa_system_sgpr_workgroup_id_z 0
		.amdhsa_system_sgpr_workgroup_info 0
		.amdhsa_system_vgpr_workitem_id 0
		.amdhsa_next_free_vgpr 92
		.amdhsa_next_free_sgpr 26
		.amdhsa_accum_offset 92
		.amdhsa_reserve_vcc 1
		.amdhsa_float_round_mode_32 0
		.amdhsa_float_round_mode_16_64 0
		.amdhsa_float_denorm_mode_32 3
		.amdhsa_float_denorm_mode_16_64 3
		.amdhsa_dx10_clamp 1
		.amdhsa_ieee_mode 1
		.amdhsa_fp16_overflow 0
		.amdhsa_tg_split 0
		.amdhsa_exception_fp_ieee_invalid_op 0
		.amdhsa_exception_fp_denorm_src 0
		.amdhsa_exception_fp_ieee_div_zero 0
		.amdhsa_exception_fp_ieee_overflow 0
		.amdhsa_exception_fp_ieee_underflow 0
		.amdhsa_exception_fp_ieee_inexact 0
		.amdhsa_exception_int_div_zero 0
	.end_amdhsa_kernel

_Z7k_layerPKfS0_S0_S0_S0_S0_S0_PfS1_S1_:
	s_load_dwordx4 s[28:31], s[0:1], 0x40
	s_load_dwordx2 s[10:11], s[0:1], 0x0
	s_load_dwordx4 s[12:15], s[0:1], 0x28
	s_load_dwordx2 s[8:9], s[0:1], 0x38
	v_cmp_lt_u32_e64 s[6:7], 63, v0
	v_cmp_gt_u32_e64 s[4:5], 64, v0
	v_mov_b32_e32 v70, 0x7fc00000
	v_lshlrev_b32_e32 v18, 2, v0
	s_and_saveexec_b64 s[16:17], s[4:5]
	s_cbranch_execz .LBB2_2
	s_load_dwordx8 s[20:27], s[0:1], 0x8
	s_waitcnt lgkmcnt(0)
	global_load_dword v48, v18, s[20:21] sc1
	global_load_dword v1, v18, s[22:23] sc1
	global_load_dword v73, v18, s[20:21] offset:256 sc1
	global_load_dword v72, v18, s[22:23] offset:256 sc1
	global_load_dword v69, v18, s[20:21] offset:512 sc1
	global_load_dword v68, v18, s[22:23] offset:512 sc1
	global_load_dword v67, v18, s[20:21] offset:768 sc1
	global_load_dword v66, v18, s[22:23] offset:768 sc1
	global_load_dword v65, v18, s[20:21] offset:1024 sc1
	global_load_dword v64, v18, s[22:23] offset:1024 sc1
	global_load_dword v63, v18, s[20:21] offset:1280 sc1
	global_load_dword v62, v18, s[22:23] offset:1280 sc1
	global_load_dword v61, v18, s[20:21] offset:1536 sc1
	global_load_dword v60, v18, s[22:23] offset:1536 sc1
	global_load_dword v53, v18, s[20:21] offset:1792 sc1
	global_load_dword v52, v18, s[22:23] offset:1792 sc1
	global_load_dword v49, v18, s[24:25]
	global_load_dword v76, v18, s[26:27]
	s_waitcnt vmcnt(16)
	v_add_f32_e32 v70, 0, v1

.LBB2_4:
	s_or_b64 exec, exec, s[2:3]
	v_lshlrev_b32_e32 v23, 2, v23
	s_waitcnt lgkmcnt(0)
	s_barrier
	s_waitcnt vmcnt(25)
	ds_read_b128 v[60:63], v23 offset:512
	ds_read_b128 v[64:67], v23 offset:528
	v_cmp_eq_u32_e32 vcc, 0, v75
	s_and_b32 s9, s9, 0xffff
	s_mov_b32 s11, 0x20000
	s_waitcnt vmcnt(16) lgkmcnt(1)
	v_mul_f32_e32 v48, v58, v60
	s_waitcnt vmcnt(0)
	v_cndmask_b32_e32 v20, 0, v20, vcc
	s_mov_b32 s10, 0x100000
	v_mfma_f32_16x16x4_f32 a[0:3], v48, v14, 0
	v_mul_f32_e32 v14, v56, v61
	v_cmp_eq_u32_e32 vcc, 0, v19
	s_nop 0
	v_mfma_f32_16x16x4_f32 a[4:7], v14, v15, 0
	v_mul_f32_e32 v14, v54, v62
	s_nop 1
	v_mfma_f32_16x16x4_f32 a[0:3], v14, v16, a[0:3]
	v_mul_f32_e32 v14, v50, v63
	s_nop 1
	v_mfma_f32_16x16x4_f32 a[4:7], v14, v17, a[4:7]
	s_waitcnt lgkmcnt(0)
	v_mul_f32_e32 v14, v46, v64
	s_nop 1
	v_mfma_f32_16x16x4_f32 a[0:3], v14, v10, a[0:3]
	v_mul_f32_e32 v10, v44, v65
	ds_read_b128 v[14:17], v23 offset:1024
	ds_read_b128 v[60:63], v23 offset:768
	ds_read_b128 v[68:71], v23 offset:1040
	ds_read_b128 v[76:79], v23 offset:784
	v_mfma_f32_16x16x4_f32 a[4:7], v10, v11, a[4:7]
	v_mul_f32_e32 v11, v42, v66
	s_waitcnt lgkmcnt(3)
	v_mul_f32_e32 v10, v59, v14
	s_waitcnt lgkmcnt(2)
	v_fmac_f32_e32 v10, v58, v60
	v_mul_f32_e32 v14, v57, v15
	v_add_f32_e32 v10, v20, v10
	v_fmac_f32_e32 v14, v56, v61
	v_add_f32_e32 v10, v14, v10
	v_mfma_f32_16x16x4_f32 a[0:3], v11, v12, a[0:3]
	v_mul_f32_e32 v11, v55, v16
	v_mul_f32_e32 v12, v36, v67
	v_fmac_f32_e32 v11, v54, v62
	ds_read_b128 v[52:55], v23 offset:544
	v_add_f32_e32 v14, v11, v10
	v_mul_f32_e32 v15, v51, v17
	v_fmac_f32_e32 v15, v50, v63
	v_mfma_f32_16x16x4_f32 a[4:7], v12, v13, a[4:7]
	ds_read_b128 v[10:13], v23 offset:560
	s_waitcnt lgkmcnt(1)
	v_mul_f32_e32 v16, v40, v52
	v_add_f32_e32 v14, v15, v14
	v_mul_f32_e32 v15, v47, v68
	v_fmac_f32_e32 v15, v46, v76
	v_add_f32_e32 v14, v14, v15
	v_mul_f32_e32 v15, v38, v53
	v_mfma_f32_16x16x4_f32 a[0:3], v16, v6, a[0:3]
	v_mul_f32_e32 v20, v34, v54
	v_mul_f32_e32 v6, v45, v69
	v_fmac_f32_e32 v6, v44, v77
	v_add_f32_e32 v6, v6, v14
	v_mul_f32_e32 v14, v43, v70
	v_fmac_f32_e32 v14, v42, v78
	v_add_f32_e32 v6, v14, v6
	v_mfma_f32_16x16x4_f32 a[4:7], v15, v7, a[4:7]
	ds_read_b128 v[14:17], v23 offset:800
	ds_read_b128 v[42:45], v23 offset:1056
	v_mul_f32_e32 v7, v37, v71
	v_fmac_f32_e32 v7, v36, v79
	v_add_f32_e32 v48, v7, v6
	v_mov_b32_e32 v6, v40
	v_mov_b32_e32 v40, v41
	v_mov_b32_e32 v41, v39
	v_mfma_f32_16x16x4_f32 a[0:3], v20, v8, a[0:3]
	v_mul_f32_e32 v8, v32, v55
	v_mov_b32_e32 v7, v38
	s_waitcnt lgkmcnt(0)
	v_mul_f32_e64 v46, v40, v42
	v_mul_f32_e64 v47, v41, v43
	v_mul_f32_e32 v11, v28, v11
	v_pk_fma_f32 v[6:7], v[6:7], v[14:15], v[46:47]
	ds_read_b128 v[36:39], v23 offset:1072
	ds_read_b128 v[40:43], v23 offset:816
	v_mfma_f32_16x16x4_f32 a[4:7], v8, v9, a[4:7]
	v_mul_f32_e32 v8, v30, v10
	v_add_f32_e32 v6, v48, v6
	v_add_f32_e32 v10, v7, v6
	v_mov_b32_e32 v7, v32
	v_mov_b32_e32 v32, v35
	v_mov_b32_e32 v6, v34
	v_mov_b32_e32 v23, v21
	v_mfma_f32_16x16x4_f32 a[0:3], v8, v2, a[0:3]
	v_mul_f32_e64 v8, v32, v44
	v_mul_f32_e64 v9, v33, v45
	v_mov_b32_e32 v20, 0
	v_fma_f32 v6, v6, v16, v8
	v_fma_f32 v7, v7, v17, v9
	v_mul_f32_e32 v9, v24, v12
	v_add_f32_e32 v2, v6, v10
	v_add_f32_e32 v8, v7, v2
	v_mov_b32_e32 v2, v30
	v_mfma_f32_16x16x4_f32 a[4:7], v11, v3, a[4:7]
	v_mov_b32_e32 v3, v28
	v_mov_b32_e32 v28, v31
	s_waitcnt lgkmcnt(1)
	v_mul_f32_e64 v6, v28, v36
	v_mul_f32_e64 v7, v29, v37
	v_mov_b32_e32 v16, v21
	s_waitcnt lgkmcnt(0)
	v_pk_fma_f32 v[2:3], v[2:3], v[40:41], v[6:7]
	v_mov_b32_e32 v17, v21
	v_add_f32_e32 v2, v8, v2
	v_mfma_f32_16x16x4_f32 a[0:3], v9, v4, a[0:3]
	v_add_f32_e32 v4, v3, v2
	v_mul_f32_e32 v8, v26, v13
	v_mov_b32_e32 v3, v26
	v_mov_b32_e32 v26, v25
	v_mov_b32_e32 v2, v24
	v_pk_mul_f32 v[6:7], v[26:27], v[38:39]
	v_mov_b32_e32 v9, v21
	v_pk_fma_f32 v[2:3], v[2:3], v[42:43], v[6:7]
	v_mfma_f32_16x16x4_f32 a[4:7], v8, v5, a[4:7]
	v_add_f32_e32 v2, v2, v4
	v_add_f32_e32 v4, v3, v2
	v_mov_b32_e32 v5, 1.0
	v_mov_b32_e32 v8, v21
	s_nop 0
	v_mfma_f32_16x16x4_f32 a[0:3], v4, v5, a[0:3]
	s_nop 3
	v_accvgpr_read_b32 v3, a7
	v_accvgpr_read_b32 v2, a6
	v_accvgpr_read_b32 v7, a5
	v_accvgpr_read_b32 v6, a4
	s_nop 1
	v_accvgpr_read_b32 v5, a3
	v_accvgpr_read_b32 v4, a2
	v_pk_add_f32 v[2:3], v[2:3], v[4:5]
	v_accvgpr_read_b32 v5, a1
	v_accvgpr_read_b32 v4, a0
	v_pk_add_f32 v[4:5], v[6:7], v[4:5]
	v_max_f32_e32 v14, 0, v2
	v_max_f32_e32 v12, 0, v4
	v_max_f32_e32 v13, 0, v5
	v_max_f32_e32 v15, 0, v3
	v_lshlrev_b32_e32 v2, 6, v22
	v_and_b32_e32 v3, 12, v1
	v_or3_b32 v2, v2, v74, v3
	v_lshlrev_b32_e32 v2, 2, v2
	buffer_store_dwordx4 v[12:15], v2, s[8:11], 0 offen sc1
	v_mul_f32_e32 v4, v12, v12
	v_mul_f32_e32 v5, v13, v13
	v_mul_f32_e32 v6, v14, v14
	v_mul_f32_e32 v7, v15, v15
	v_and_b32_e32 v8, 3, v19
	v_and_b32_e32 v9, 12, v1
	v_or3_b32 v8, v8, v9, v74
	s_lshl_b32 s2, s12, 8
	v_lshl_add_u32 v8, v8, 2, s2
	v_add_f32_dpp v12, v12, v12 quad_perm:[1,0,3,2] row_mask:0xf bank_mask:0xf
	v_add_f32_dpp v13, v13, v13 quad_perm:[1,0,3,2] row_mask:0xf bank_mask:0xf
	v_add_f32_dpp v14, v14, v14 quad_perm:[1,0,3,2] row_mask:0xf bank_mask:0xf
	v_add_f32_dpp v15, v15, v15 quad_perm:[1,0,3,2] row_mask:0xf bank_mask:0xf
	v_add_f32_dpp v4, v4, v4 quad_perm:[1,0,3,2] row_mask:0xf bank_mask:0xf
	v_add_f32_dpp v5, v5, v5 quad_perm:[1,0,3,2] row_mask:0xf bank_mask:0xf
	v_add_f32_dpp v6, v6, v6 quad_perm:[1,0,3,2] row_mask:0xf bank_mask:0xf
	v_add_f32_dpp v7, v7, v7 quad_perm:[1,0,3,2] row_mask:0xf bank_mask:0xf
	v_add_f32_dpp v12, v12, v12 quad_perm:[2,3,0,1] row_mask:0xf bank_mask:0xf
	v_add_f32_dpp v13, v13, v13 quad_perm:[2,3,0,1] row_mask:0xf bank_mask:0xf
	v_add_f32_dpp v14, v14, v14 quad_perm:[2,3,0,1] row_mask:0xf bank_mask:0xf
	v_add_f32_dpp v15, v15, v15 quad_perm:[2,3,0,1] row_mask:0xf bank_mask:0xf
	v_add_f32_dpp v4, v4, v4 quad_perm:[2,3,0,1] row_mask:0xf bank_mask:0xf
	v_add_f32_dpp v5, v5, v5 quad_perm:[2,3,0,1] row_mask:0xf bank_mask:0xf
	v_add_f32_dpp v6, v6, v6 quad_perm:[2,3,0,1] row_mask:0xf bank_mask:0xf
	v_add_f32_dpp v7, v7, v7 quad_perm:[2,3,0,1] row_mask:0xf bank_mask:0xf
	v_add_f32_dpp v12, v12, v12 row_half_mirror row_mask:0xf bank_mask:0xf
	v_add_f32_dpp v13, v13, v13 row_half_mirror row_mask:0xf bank_mask:0xf
	v_add_f32_dpp v14, v14, v14 row_half_mirror row_mask:0xf bank_mask:0xf
	v_add_f32_dpp v15, v15, v15 row_half_mirror row_mask:0xf bank_mask:0xf
	v_add_f32_dpp v4, v4, v4 row_half_mirror row_mask:0xf bank_mask:0xf
	v_add_f32_dpp v5, v5, v5 row_half_mirror row_mask:0xf bank_mask:0xf
	v_add_f32_dpp v6, v6, v6 row_half_mirror row_mask:0xf bank_mask:0xf
	v_add_f32_dpp v7, v7, v7 row_half_mirror row_mask:0xf bank_mask:0xf
	v_add_f32_dpp v12, v12, v12 row_mirror row_mask:0xf bank_mask:0xf
	v_add_f32_dpp v13, v13, v13 row_mirror row_mask:0xf bank_mask:0xf
	v_add_f32_dpp v14, v14, v14 row_mirror row_mask:0xf bank_mask:0xf
	v_add_f32_dpp v15, v15, v15 row_mirror row_mask:0xf bank_mask:0xf
	v_add_f32_dpp v4, v4, v4 row_mirror row_mask:0xf bank_mask:0xf
	v_add_f32_dpp v5, v5, v5 row_mirror row_mask:0xf bank_mask:0xf
	v_add_f32_dpp v6, v6, v6 row_mirror row_mask:0xf bank_mask:0xf
	v_add_f32_dpp v7, v7, v7 row_mirror row_mask:0xf bank_mask:0xf
	s_mov_b32 s32, 0x00020002
	s_mov_b32 s33, 0x00020002
	v_cndmask_b32_e64 v12, v12, v13, s[32:33]
	s_mov_b32 s32, 0x00040004
	s_mov_b32 s33, 0x00040004
	v_cndmask_b32_e64 v12, v12, v14, s[32:33]
	s_mov_b32 s32, 0x00080008
	s_mov_b32 s33, 0x00080008
	v_cndmask_b32_e64 v12, v12, v15, s[32:33]
	s_mov_b32 s32, 0x00100010
	s_mov_b32 s33, 0x00100010
	v_cndmask_b32_e64 v12, v12, v4, s[32:33]
	s_mov_b32 s32, 0x00200020
	s_mov_b32 s33, 0x00200020
	v_cndmask_b32_e64 v12, v12, v5, s[32:33]
	s_mov_b32 s32, 0x00400040
	s_mov_b32 s33, 0x00400040
	v_cndmask_b32_e64 v12, v12, v6, s[32:33]
	s_mov_b32 s32, 0x00800080
	s_mov_b32 s33, 0x00800080
	v_cndmask_b32_e64 v12, v12, v7, s[32:33]
	s_mov_b32 s2, 0x000f000f
	s_mov_b32 s3, 0x000f000f
	s_mov_b64 exec, s[2:3]
	global_atomic_add_f32 v8, v12, s[28:29]
	s_mov_b32 s2, 0x00f000f0
	s_mov_b32 s3, 0x00f000f0
	s_mov_b64 exec, s[2:3]
	global_atomic_add_f32 v8, v12, s[30:31]
	s_endpgm

	.amdhsa_kernel _Z7k_layerPKfS0_S0_S0_S0_S0_S0_PfS1_S1_
		.amdhsa_group_segment_fixed_size 1280
		.amdhsa_private_segment_fixed_size 0
		.amdhsa_kernarg_size 80
		.amdhsa_user_sgpr_count 2
		.amdhsa_user_sgpr_dispatch_ptr 0
		.amdhsa_user_sgpr_queue_ptr 0
		.amdhsa_user_sgpr_kernarg_segment_ptr 1
		.amdhsa_user_sgpr_dispatch_id 0
		.amdhsa_user_sgpr_kernarg_preload_length 0
		.amdhsa_user_sgpr_kernarg_preload_offset 0
		.amdhsa_user_sgpr_private_segment_size 0
		.amdhsa_uses_dynamic_stack 0
		.amdhsa_enable_private_segment 0
		.amdhsa_system_sgpr_workgroup_id_x 1
		.amdhsa_system_sgpr_workgroup_id_y 0
		.amdhsa_system_sgpr_workgroup_id_z 0
		.amdhsa_system_sgpr_workgroup_info 0
		.amdhsa_system_vgpr_workitem_id 0
		.amdhsa_next_free_vgpr 88
		.amdhsa_next_free_sgpr 34
		.amdhsa_accum_offset 80
		.amdhsa_reserve_vcc 1
		.amdhsa_float_round_mode_32 0
		.amdhsa_float_round_mode_16_64 0
		.amdhsa_float_denorm_mode_32 3
		.amdhsa_float_denorm_mode_16_64 3
		.amdhsa_dx10_clamp 1
		.amdhsa_ieee_mode 1
		.amdhsa_fp16_overflow 0
		.amdhsa_tg_split 0
		.amdhsa_exception_fp_ieee_invalid_op 0
		.amdhsa_exception_fp_denorm_src 0
		.amdhsa_exception_fp_ieee_div_zero 0
		.amdhsa_exception_fp_ieee_overflow 0
		.amdhsa_exception_fp_ieee_underflow 0
		.amdhsa_exception_fp_ieee_inexact 0
		.amdhsa_exception_int_div_zero 0
	.end_amdhsa_kernel

_Z8k5_finalPKfS0_S0_S0_S0_S0_S0_S0_S0_Pf:
	s_load_dwordx8 s[4:11], s[0:1], 0x28
	s_load_dwordx2 s[12:13], s[0:1], 0x0
	s_load_dwordx8 s[16:23], s[0:1], 0x8
	v_lshrrev_b32_e32 v63, 4, v0
	v_lshlrev_b32_e32 v63, 2, v63
	v_cmp_gt_u32_e32 vcc, 64, v0
	v_mov_b32_e32 v54, 0x7fc00000
	v_lshlrev_b32_e32 v58, 2, v0
	v_mov_b32_e32 v55, 0x7fc00000
	s_waitcnt lgkmcnt(0)
	global_load_dword v63, v63, s[10:11]
	s_and_saveexec_b64 s[14:15], vcc
	s_cbranch_execz .LBB3_2
	global_load_dword v3, v58, s[16:17] sc1
	global_load_dword v2, v58, s[18:19] sc1
	global_load_dword v53, v58, s[16:17] offset:256 sc1
	global_load_dword v52, v58, s[18:19] offset:256 sc1
	global_load_dword v51, v58, s[16:17] offset:512 sc1
	global_load_dword v50, v58, s[18:19] offset:512 sc1
	global_load_dword v49, v58, s[16:17] offset:768 sc1
	global_load_dword v48, v58, s[18:19] offset:768 sc1
	global_load_dword v47, v58, s[16:17] offset:1024 sc1
	global_load_dword v46, v58, s[18:19] offset:1024 sc1
	global_load_dword v45, v58, s[16:17] offset:1280 sc1
	global_load_dword v44, v58, s[18:19] offset:1280 sc1
	global_load_dword v43, v58, s[16:17] offset:1536 sc1
	global_load_dword v42, v58, s[18:19] offset:1536 sc1
	global_load_dword v41, v58, s[16:17] offset:1792 sc1
	global_load_dword v40, v58, s[18:19] offset:1792 sc1
	global_load_dword v61, v58, s[20:21]
	global_load_dword v60, v58, s[22:23]
	s_waitcnt vmcnt(16)
	v_pk_add_f32 v[54:55], v[2:3], 0 op_sel_hi:[1,0]

.LBB3_4:
	s_or_b64 exec, exec, s[2:3]
	v_lshlrev_b32_e32 v38, 2, v38
	s_waitcnt lgkmcnt(0)
	s_barrier
	s_waitcnt vmcnt(12)
	ds_read_b128 v[40:43], v38 offset:4096
	ds_read_b128 v[44:47], v38 offset:4112
	v_cmp_eq_u32_e32 vcc, 0, v59
	v_lshlrev_b32_e32 v1, 10, v1
	s_ashr_i32 s4, s14, 5
	s_waitcnt vmcnt(6) lgkmcnt(1)
	v_mul_f32_e32 v40, v22, v40
	s_and_b32 s2, s14, 0x1f0
	s_mov_b32 s3, 0
	s_waitcnt vmcnt(2)
	v_mfma_f32_16x16x4_f32 a[0:3], v40, v34, 0
	v_mul_f32_e32 v34, v23, v41
	s_waitcnt vmcnt(0)
	v_cndmask_b32_e32 v40, 0, v62, vcc
	s_lshl_b32 s2, s2, 2
	v_mfma_f32_16x16x4_f32 a[4:7], v34, v35, 0
	v_mul_f32_e32 v34, v24, v42
	s_nop 1
	v_mfma_f32_16x16x4_f32 a[0:3], v34, v36, a[0:3]
	v_mul_f32_e32 v34, v25, v43
	s_nop 1
	v_mfma_f32_16x16x4_f32 a[4:7], v34, v37, a[4:7]
	s_waitcnt lgkmcnt(0)
	v_mul_f32_e32 v34, v18, v44
	s_nop 1
	v_mfma_f32_16x16x4_f32 a[0:3], v34, v30, a[0:3]
	v_mul_f32_e32 v30, v19, v45
	s_nop 1
	v_mfma_f32_16x16x4_f32 a[4:7], v30, v31, a[4:7]
	v_mul_f32_e32 v30, v20, v46
	s_nop 1
	v_mfma_f32_16x16x4_f32 a[0:3], v30, v32, a[0:3]
	v_mul_f32_e32 v30, v21, v47
	s_nop 1
	v_mfma_f32_16x16x4_f32 a[4:7], v30, v33, a[4:7]
	ds_read_b128 v[30:33], v38 offset:4128
	ds_read_b128 v[34:37], v38 offset:4144
	s_waitcnt lgkmcnt(1)
	v_mul_f32_e32 v30, v10, v30
	s_waitcnt lgkmcnt(0)
	v_mul_f32_e32 v34, v6, v34
	v_mfma_f32_16x16x4_f32 a[0:3], v30, v26, a[0:3]
	v_mul_f32_e32 v26, v11, v31
	s_nop 1
	v_mfma_f32_16x16x4_f32 a[4:7], v26, v27, a[4:7]
	v_mul_f32_e32 v26, v12, v32
	s_nop 1
	v_mfma_f32_16x16x4_f32 a[0:3], v26, v28, a[0:3]
	v_mul_f32_e32 v26, v13, v33
	ds_read_b128 v[30:33], v38 offset:4368
	s_waitcnt lgkmcnt(0)
	v_mul_f32_e32 v19, v19, v31
	v_mfma_f32_16x16x4_f32 a[4:7], v26, v29, a[4:7]
	ds_read_b128 v[26:29], v38 offset:4352
	v_fmac_f32_e32 v19, v18, v30
	v_fmac_f32_e32 v19, v20, v32
	v_fmac_f32_e32 v19, v21, v33
	s_waitcnt lgkmcnt(0)
	v_mul_f32_e32 v23, v23, v27
	v_fmac_f32_e32 v23, v22, v26
	v_mfma_f32_16x16x4_f32 a[0:3], v34, v14, a[0:3]
	v_mul_f32_e32 v14, v7, v35
	v_fmac_f32_e32 v23, v24, v28
	v_fmac_f32_e32 v23, v25, v29
	v_add_f32_e32 v26, v40, v23
	ds_read_b128 v[22:25], v38 offset:4384
	v_mfma_f32_16x16x4_f32 a[4:7], v14, v15, a[4:7]
	v_add_f32_e32 v15, v26, v19
	ds_read_b128 v[18:21], v38 offset:4400
	v_mul_f32_e32 v14, v8, v36
	s_waitcnt lgkmcnt(1)
	v_mul_f32_e32 v11, v11, v23
	v_fmac_f32_e32 v11, v10, v22
	v_fmac_f32_e32 v11, v12, v24
	s_waitcnt lgkmcnt(0)
	v_mul_f32_e32 v7, v7, v19
	v_mfma_f32_16x16x4_f32 a[0:3], v14, v16, a[0:3]
	v_fmac_f32_e32 v7, v6, v18
	v_fmac_f32_e32 v11, v13, v25
	v_fmac_f32_e32 v7, v8, v20
	v_add_f32_e32 v11, v15, v11
	v_fmac_f32_e32 v7, v9, v21
	v_mul_f32_e32 v10, v9, v37
	v_add_f32_e32 v6, v11, v7
	v_mov_b32_e32 v7, 1.0
	v_mfma_f32_16x16x4_f32 a[4:7], v10, v17, a[4:7]
	v_lshlrev_b32_e32 v38, 2, v56
	v_mfma_f32_16x16x4_f32 a[0:3], v6, v7, a[0:3]
	s_nop 7
	v_accvgpr_read_b32 v9, a5
	v_accvgpr_read_b32 v8, a4
	v_accvgpr_read_b32 v7, a1
	v_accvgpr_read_b32 v6, a0
	v_pk_add_f32 v[6:7], v[8:9], v[6:7]
	s_nop 0
	v_max_f32_e32 v6, 0, v6
	s_nop 1
	v_mfma_f32_16x16x4_f32 a[8:11], v2, v6, 0
	v_max_f32_e32 v2, 0, v7
	v_accvgpr_read_b32 v7, a3
	v_accvgpr_read_b32 v6, a2
	v_mfma_f32_16x16x4_f32 a[8:11], v3, v2, a[8:11]
	v_accvgpr_read_b32 v3, a7
	v_accvgpr_read_b32 v2, a6
	v_add_f32_e64 v2, v2, v6
	v_add_f32_e64 v3, v3, v7
	v_max_f32_e32 v2, 0, v2
	s_nop 1
	v_mfma_f32_16x16x4_f32 a[0:3], v4, v2, a[8:11]
	v_max_f32_e32 v2, 0, v3
	v_lshlrev_b32_e32 v3, 6, v57
	v_or3_b32 v1, v1, v3, v38
	v_mfma_f32_16x16x4_f32 a[0:3], v5, v2, a[0:3]
	s_nop 9
	ds_write_b32 v1, a0
	ds_write_b32 v1, a1 offset:64
	ds_write_b32 v1, a2 offset:128
	ds_write_b32 v1, a3 offset:192
	v_lshlrev_b32_e32 v1, 2, v0
	s_waitcnt lgkmcnt(0)
	s_barrier
	v_lshl_or_b32 v2, v0, 6, v38
	ds_read2st64_b32 v[8:9], v2 offset1:4
	ds_read2st64_b32 v[2:3], v2 offset0:8 offset1:12
	v_and_or_b32 v0, s4, -16, v0
	v_ashrrev_i32_e32 v1, 31, v0
	v_lshlrev_b64 v[0:1], 11, v[0:1]
	s_waitcnt lgkmcnt(1)
	v_mov_b32_e32 v4, v8
	s_waitcnt lgkmcnt(0)
	v_mov_b32_e32 v5, v2
	v_mov_b32_e32 v2, v9
	v_lshl_add_u64 v[0:1], s[0:1], 0, v[0:1]
	v_pk_add_f32 v[2:3], v[4:5], v[2:3]
	v_lshl_add_u64 v[0:1], v[0:1], 0, s[2:3]
	v_add_f32_e32 v2, v2, v3
	v_lshl_add_u64 v[0:1], v[0:1], 0, v[38:39]
	s_waitcnt vmcnt(0)
	v_add_f32_e32 v2, v63, v2
	global_store_dword v[0:1], v2, off
	s_endpgm

amdhsa.kernels:
  - .agpr_count:     0
    .args:
      - .actual_access:  read_only
        .address_space:  global
        .offset:         0
        .size:           8
        .value_kind:     global_buffer
      - .actual_access:  write_only
        .address_space:  global
        .offset:         8
        .size:           8
        .value_kind:     global_buffer
      - .offset:         16
        .size:           64
        .value_kind:     by_value
    .group_segment_fixed_size: 8224
    .kernarg_segment_align: 8
    .kernarg_segment_size: 80
    .language:       OpenCL C
    .language_version:
      - 2
      - 0
    .max_flat_workgroup_size: 256
    .name:           _Z9k1_streamPKfPf6PfArgs
    .private_segment_fixed_size: 0
    .sgpr_count:     28
    .sgpr_spill_count: 0
    .symbol:         _Z9k1_streamPKfPf6PfArgs.kd
    .uniform_work_group_size: 1
    .uses_dynamic_stack: false
    .vgpr_count:     72
    .vgpr_spill_count: 0
    .wavefront_size: 64
  - .agpr_count:     0
    .args:
      - .actual_access:  read_only
        .address_space:  global
        .offset:         0
        .size:           8
        .value_kind:     global_buffer
      - .actual_access:  read_only
        .address_space:  global
        .offset:         8
        .size:           8
        .value_kind:     global_buffer
      - .actual_access:  read_only
        .address_space:  global
        .offset:         16
        .size:           8
        .value_kind:     global_buffer
      - .actual_access:  write_only
        .address_space:  global
        .offset:         24
        .size:           8
        .value_kind:     global_buffer
      - .address_space:  global
        .offset:         32
        .size:           8
        .value_kind:     global_buffer
      - .address_space:  global
        .offset:         40
        .size:           8
        .value_kind:     global_buffer
    .group_segment_fixed_size: 3712
    .kernarg_segment_align: 8
    .kernarg_segment_size: 48
    .language:       OpenCL C
    .language_version:
      - 2
      - 0
    .max_flat_workgroup_size: 256
    .name:           _Z9k2_layer1PKfS0_S0_PfS1_S1_
    .private_segment_fixed_size: 0
    .sgpr_count:     32
    .sgpr_spill_count: 0
    .symbol:         _Z9k2_layer1PKfS0_S0_PfS1_S1_.kd
    .uniform_work_group_size: 1
    .uses_dynamic_stack: false
    .vgpr_count:     92
    .vgpr_spill_count: 0
    .wavefront_size: 64
  - .agpr_count:     8
    .args:
      - .actual_access:  read_only
        .address_space:  global
        .offset:         0
        .size:           8
        .value_kind:     global_buffer
      - .actual_access:  read_only
        .address_space:  global
        .offset:         8
        .size:           8
        .value_kind:     global_buffer
      - .actual_access:  read_only
        .address_space:  global
        .offset:         16
        .size:           8
        .value_kind:     global_buffer
      - .actual_access:  read_only
        .address_space:  global
        .offset:         24
        .size:           8
        .value_kind:     global_buffer
      - .actual_access:  read_only
        .address_space:  global
        .offset:         32
        .size:           8
        .value_kind:     global_buffer
      - .actual_access:  read_only
        .address_space:  global
        .offset:         40
        .size:           8
        .value_kind:     global_buffer
      - .actual_access:  read_only
        .address_space:  global
        .offset:         48
        .size:           8
        .value_kind:     global_buffer
      - .actual_access:  write_only
        .address_space:  global
        .offset:         56
        .size:           8
        .value_kind:     global_buffer
      - .address_space:  global
        .offset:         64
        .size:           8
        .value_kind:     global_buffer
      - .address_space:  global
        .offset:         72
        .size:           8
        .value_kind:     global_buffer
    .group_segment_fixed_size: 1280
    .kernarg_segment_align: 8
    .kernarg_segment_size: 80
    .language:       OpenCL C
    .language_version:
      - 2
      - 0
    .max_flat_workgroup_size: 256
    .name:           _Z7k_layerPKfS0_S0_S0_S0_S0_S0_PfS1_S1_
    .private_segment_fixed_size: 0
    .sgpr_count:     40
    .sgpr_spill_count: 0
    .symbol:         _Z7k_layerPKfS0_S0_S0_S0_S0_S0_PfS1_S1_.kd
    .uniform_work_group_size: 1
    .uses_dynamic_stack: false
    .vgpr_count:     88
    .vgpr_spill_count: 0
    .wavefront_size: 64
  - .agpr_count:     12
    .args:
      - .actual_access:  read_only
        .address_space:  global
        .offset:         0
        .size:           8
        .value_kind:     global_buffer
      - .actual_access:  read_only
        .address_space:  global
        .offset:         8
        .size:           8
        .value_kind:     global_buffer
      - .actual_access:  read_only
        .address_space:  global
        .offset:         16
        .size:           8
        .value_kind:     global_buffer
      - .actual_access:  read_only
        .address_space:  global
        .offset:         24
        .size:           8
        .value_kind:     global_buffer
      - .actual_access:  read_only
        .address_space:  global
        .offset:         32
        .size:           8
        .value_kind:     global_buffer
      - .actual_access:  read_only
        .address_space:  global
        .offset:         40
        .size:           8
        .value_kind:     global_buffer
      - .actual_access:  read_only
        .address_space:  global
        .offset:         48
        .size:           8
        .value_kind:     global_buffer
      - .actual_access:  read_only
        .address_space:  global
        .offset:         56
        .size:           8
        .value_kind:     global_buffer
      - .actual_access:  read_only
        .address_space:  global
        .offset:         64
        .size:           8
        .value_kind:     global_buffer
      - .actual_access:  write_only
        .address_space:  global
        .offset:         72
        .size:           8
        .value_kind:     global_buffer
    .group_segment_fixed_size: 4608
    .kernarg_segment_align: 8
    .kernarg_segment_size: 80
    .language:       OpenCL C
    .language_version:
      - 2
      - 0
    .max_flat_workgroup_size: 256
    .name:           _Z8k5_finalPKfS0_S0_S0_S0_S0_S0_S0_S0_Pf
    .private_segment_fixed_size: 0
    .sgpr_count:     30
    .sgpr_spill_count: 0
    .symbol:         _Z8k5_finalPKfS0_S0_S0_S0_S0_S0_S0_S0_Pf.kd
    .uniform_work_group_size: 1
    .uses_dynamic_stack: false
    .vgpr_count:     76
    .vgpr_spill_count: 0
    .wavefront_size: 64
